# v24 + expert gate/up GEMM: half-workgroup epilogues no longer barrier-aligned (leading half's SwiGLU epilogue overlaps the trailing half's last MFMA block; template's ALIGN_EPI=false barrier protocol)
# speedup vs baseline: 1.0095x; 1.0095x over previous
.LBB0_663:
	v_pk_mul_f32 v[102:103], v[26:27], v[102:103]
	v_pk_mul_f32 v[26:27], v[26:27], s[20:21] op_sel_hi:[1,0]
	v_pk_mul_f32 v[146:147], v[0:1], s[20:21] op_sel_hi:[1,0]
	v_exp_f32_e32 v26, v26
	v_exp_f32_e32 v27, v27
	v_pk_mul_f32 v[126:127], v[2:3], v[126:127]
	v_pk_mul_f32 v[0:1], v[0:1], v[124:125]
	v_pk_mul_f32 v[2:3], v[2:3], s[20:21] op_sel_hi:[1,0]
	v_pk_fma_f32 v[26:27], v[26:27], s[22:23], s[22:23] op_sel_hi:[1,0,0]
	v_pk_mul_f32 v[124:125], v[4:5], s[20:21] op_sel_hi:[1,0]
	v_rcp_f32_e32 v26, v26
	v_rcp_f32_e32 v27, v27
	v_pk_mul_f32 v[122:123], v[6:7], v[122:123]
	v_pk_mul_f32 v[4:5], v[4:5], v[120:121]
	v_pk_mul_f32 v[6:7], v[6:7], s[20:21] op_sel_hi:[1,0]
	v_pk_mul_f32 v[120:121], v[8:9], s[20:21] op_sel_hi:[1,0]
	v_pk_mul_f32 v[118:119], v[10:11], v[118:119]
	v_pk_mul_f32 v[8:9], v[8:9], v[116:117]
	v_pk_mul_f32 v[10:11], v[10:11], s[20:21] op_sel_hi:[1,0]
	v_pk_mul_f32 v[116:117], v[12:13], s[20:21] op_sel_hi:[1,0]
	v_pk_mul_f32 v[114:115], v[14:15], v[114:115]
	v_pk_mul_f32 v[12:13], v[12:13], v[112:113]
	v_pk_mul_f32 v[14:15], v[14:15], s[20:21] op_sel_hi:[1,0]
	v_pk_mul_f32 v[112:113], v[16:17], s[20:21] op_sel_hi:[1,0]
	v_pk_mul_f32 v[110:111], v[18:19], v[110:111]
	v_pk_mul_f32 v[16:17], v[16:17], v[108:109]
	v_pk_mul_f32 v[18:19], v[18:19], s[20:21] op_sel_hi:[1,0]
	v_pk_mul_f32 v[108:109], v[20:21], s[20:21] op_sel_hi:[1,0]
	v_pk_mul_f32 v[106:107], v[22:23], v[106:107]
	v_pk_mul_f32 v[20:21], v[20:21], v[104:105]
	v_pk_mul_f32 v[22:23], v[22:23], s[20:21] op_sel_hi:[1,0]
	v_pk_mul_f32 v[104:105], v[24:25], s[20:21] op_sel_hi:[1,0]
	v_pk_mul_f32 v[24:25], v[24:25], v[100:101]
	v_pk_mul_f32 v[100:101], v[28:29], s[20:21] op_sel_hi:[1,0]
	v_pk_mul_f32 v[26:27], v[26:27], v[102:103]
	v_pk_mul_f32 v[102:103], v[30:31], s[20:21] op_sel_hi:[1,0]
	v_exp_f32_e32 v146, v146
	v_exp_f32_e32 v147, v147
	v_exp_f32_e32 v2, v2
	v_exp_f32_e32 v3, v3
	v_exp_f32_e32 v124, v124
	v_exp_f32_e32 v125, v125
	v_exp_f32_e32 v6, v6
	v_exp_f32_e32 v7, v7
	v_exp_f32_e32 v120, v120
	v_exp_f32_e32 v121, v121
	v_exp_f32_e32 v10, v10
	v_exp_f32_e32 v11, v11
	v_exp_f32_e32 v116, v116
	v_exp_f32_e32 v117, v117
	v_exp_f32_e32 v14, v14
	v_exp_f32_e32 v15, v15
	v_exp_f32_e32 v112, v112
	v_exp_f32_e32 v113, v113
	v_exp_f32_e32 v18, v18
	v_exp_f32_e32 v19, v19
	v_exp_f32_e32 v108, v108
	v_exp_f32_e32 v109, v109
	v_exp_f32_e32 v22, v22
	v_exp_f32_e32 v23, v23
	v_exp_f32_e32 v104, v104
	v_exp_f32_e32 v105, v105
	v_exp_f32_e32 v100, v100
	v_exp_f32_e32 v101, v101
	v_exp_f32_e32 v102, v102
	v_exp_f32_e32 v103, v103
	s_mul_hi_i32 s48, s45, 0x2e8ba2e9
	s_lshr_b32 s49, s48, 31
	s_ashr_i32 s48, s48, 2
	s_add_i32 s48, s48, s49
	v_pk_fma_f32 v[146:147], v[146:147], s[22:23], s[22:23] op_sel_hi:[1,0,0]
	v_pk_fma_f32 v[2:3], v[2:3], s[22:23], s[22:23] op_sel_hi:[1,0,0]
	v_pk_fma_f32 v[124:125], v[124:125], s[22:23], s[22:23] op_sel_hi:[1,0,0]
	v_pk_fma_f32 v[6:7], v[6:7], s[22:23], s[22:23] op_sel_hi:[1,0,0]
	v_pk_fma_f32 v[120:121], v[120:121], s[22:23], s[22:23] op_sel_hi:[1,0,0]
	v_pk_fma_f32 v[10:11], v[10:11], s[22:23], s[22:23] op_sel_hi:[1,0,0]
	v_pk_fma_f32 v[116:117], v[116:117], s[22:23], s[22:23] op_sel_hi:[1,0,0]
	v_pk_fma_f32 v[14:15], v[14:15], s[22:23], s[22:23] op_sel_hi:[1,0,0]
	v_pk_fma_f32 v[112:113], v[112:113], s[22:23], s[22:23] op_sel_hi:[1,0,0]
	v_pk_fma_f32 v[18:19], v[18:19], s[22:23], s[22:23] op_sel_hi:[1,0,0]
	v_pk_fma_f32 v[108:109], v[108:109], s[22:23], s[22:23] op_sel_hi:[1,0,0]
	v_pk_fma_f32 v[22:23], v[22:23], s[22:23], s[22:23] op_sel_hi:[1,0,0]
	v_pk_fma_f32 v[104:105], v[104:105], s[22:23], s[22:23] op_sel_hi:[1,0,0]
	v_pk_fma_f32 v[100:101], v[100:101], s[22:23], s[22:23] op_sel_hi:[1,0,0]
	v_pk_mul_f32 v[28:29], v[28:29], v[96:97]
	v_pk_fma_f32 v[96:97], v[102:103], s[22:23], s[22:23] op_sel_hi:[1,0,0]
	s_mul_i32 s48, s48, 22
	v_rcp_f32_e32 v146, v146
	v_rcp_f32_e32 v147, v147
	v_rcp_f32_e32 v2, v2
	v_rcp_f32_e32 v3, v3
	v_rcp_f32_e32 v124, v124
	v_rcp_f32_e32 v125, v125
	v_rcp_f32_e32 v6, v6
	v_rcp_f32_e32 v7, v7
	v_rcp_f32_e32 v120, v120
	v_rcp_f32_e32 v121, v121
	v_rcp_f32_e32 v10, v10
	v_rcp_f32_e32 v11, v11
	v_rcp_f32_e32 v116, v116
	v_rcp_f32_e32 v117, v117
	v_rcp_f32_e32 v14, v14
	v_rcp_f32_e32 v15, v15
	v_rcp_f32_e32 v112, v112
	v_rcp_f32_e32 v113, v113
	v_rcp_f32_e32 v18, v18
	v_rcp_f32_e32 v19, v19
	v_rcp_f32_e32 v108, v108
	v_rcp_f32_e32 v109, v109
	v_rcp_f32_e32 v22, v22
	v_rcp_f32_e32 v23, v23
	v_rcp_f32_e32 v104, v104
	v_rcp_f32_e32 v105, v105
	v_rcp_f32_e32 v100, v100
	v_rcp_f32_e32 v101, v101
	v_rcp_f32_e32 v96, v96
	v_rcp_f32_e32 v97, v97
	s_sub_i32 s45, s45, s48
	s_mul_hi_i32 s47, s46, 22
	s_mul_i32 s46, s46, 22
	s_ashr_i32 s48, s45, 31
	s_add_u32 s45, s46, s45
	v_pk_mul_f32 v[30:31], v[30:31], v[98:99]
	s_addc_u32 s46, s47, s48
	v_pk_mul_f32 v[0:1], v[146:147], v[0:1]
	v_pk_mul_f32 v[2:3], v[2:3], v[126:127]
	v_pk_mul_f32 v[4:5], v[124:125], v[4:5]
	v_pk_mul_f32 v[6:7], v[6:7], v[122:123]
	v_pk_mul_f32 v[8:9], v[120:121], v[8:9]
	v_pk_mul_f32 v[10:11], v[10:11], v[118:119]
	v_pk_mul_f32 v[12:13], v[116:117], v[12:13]
	v_pk_mul_f32 v[14:15], v[14:15], v[114:115]
	v_pk_mul_f32 v[16:17], v[112:113], v[16:17]
	v_pk_mul_f32 v[18:19], v[18:19], v[110:111]
	v_pk_mul_f32 v[20:21], v[108:109], v[20:21]
	v_pk_mul_f32 v[22:23], v[22:23], v[106:107]
	v_pk_mul_f32 v[24:25], v[104:105], v[24:25]
	v_pk_mul_f32 v[28:29], v[100:101], v[28:29]
	v_pk_mul_f32 v[30:31], v[96:97], v[30:31]
	s_mulk_i32 s46, 0x6000
	s_mul_hi_u32 s47, s45, 0x6000
	v_med3_f32 v0, v0, s40, v145
	v_med3_f32 v1, v1, s40, v145
	v_med3_f32 v2, v2, s40, v145
	v_med3_f32 v3, v3, s40, v145
	v_med3_f32 v4, v4, s40, v145
	v_med3_f32 v5, v5, s40, v145
	v_med3_f32 v6, v6, s40, v145
	v_med3_f32 v7, v7, s40, v145
	v_med3_f32 v8, v8, s40, v145
	v_med3_f32 v9, v9, s40, v145
	v_med3_f32 v10, v10, s40, v145
	v_med3_f32 v11, v11, s40, v145
	v_med3_f32 v12, v12, s40, v145
	v_med3_f32 v13, v13, s40, v145
	v_med3_f32 v14, v14, s40, v145
	v_med3_f32 v15, v15, s40, v145
	v_med3_f32 v16, v16, s40, v145
	v_med3_f32 v17, v17, s40, v145
	v_med3_f32 v18, v18, s40, v145
	v_med3_f32 v19, v19, s40, v145
	v_med3_f32 v20, v20, s40, v145
	v_med3_f32 v21, v21, s40, v145
	v_med3_f32 v22, v22, s40, v145
	v_med3_f32 v23, v23, s40, v145
	v_med3_f32 v24, v24, s40, v145
	v_med3_f32 v25, v25, s40, v145
	v_med3_f32 v26, v26, s40, v145
	v_med3_f32 v27, v27, s40, v145
	v_med3_f32 v28, v28, s40, v145
	v_med3_f32 v29, v29, s40, v145
	v_med3_f32 v30, v30, s40, v145
	v_med3_f32 v31, v31, s40, v145
	s_add_i32 s47, s47, s46
	s_mulk_i32 s45, 0x6000
	v_permlane32_swap_b32_e32 v0, v16
	v_permlane32_swap_b32_e32 v8, v24
	v_permlane32_swap_b32_e32 v1, v17
	v_permlane32_swap_b32_e32 v9, v25
	v_permlane32_swap_b32_e32 v2, v18
	v_permlane32_swap_b32_e32 v10, v26
	v_permlane32_swap_b32_e32 v3, v19
	v_permlane32_swap_b32_e32 v11, v27
	v_permlane32_swap_b32_e32 v4, v20
	v_permlane32_swap_b32_e32 v12, v28
	v_permlane32_swap_b32_e32 v5, v21
	v_permlane32_swap_b32_e32 v13, v29
	v_permlane32_swap_b32_e32 v6, v22
	v_permlane32_swap_b32_e32 v14, v30
	v_permlane32_swap_b32_e32 v7, v23
	v_permlane32_swap_b32_e32 v15, v31
	s_add_u32 s46, s29, s45
	v_permlane16_swap_b32_e32 v0, v8
	v_permlane16_swap_b32_e32 v16, v24
	v_permlane16_swap_b32_e32 v1, v9
	v_permlane16_swap_b32_e32 v17, v25
	v_permlane16_swap_b32_e32 v2, v10
	v_permlane16_swap_b32_e32 v18, v26
	v_permlane16_swap_b32_e32 v3, v11
	v_permlane16_swap_b32_e32 v19, v27
	v_permlane16_swap_b32_e32 v4, v12
	v_permlane16_swap_b32_e32 v20, v28
	v_permlane16_swap_b32_e32 v5, v13
	v_permlane16_swap_b32_e32 v21, v29
	v_permlane16_swap_b32_e32 v6, v14
	v_permlane16_swap_b32_e32 v22, v30
	v_permlane16_swap_b32_e32 v7, v15
	v_permlane16_swap_b32_e32 v23, v31
	s_addc_u32 s47, s30, s47
	v_cvt_scalef32_2xpk16_fp6_f32 v[0:5], v[0:15], v[16:31], 1.0
	v_lshl_add_u64 v[98:99], s[46:47], 0, v[128:129]
	global_store_dwordx4 v[98:99], v[0:3], off
	v_pk_mul_f32 v[6:7], v[90:91], s[20:21] op_sel_hi:[1,0]
	v_lshl_add_u64 v[96:97], s[46:47], 0, v[130:131]
	v_pk_mul_f32 v[0:1], v[88:89], s[20:21] op_sel_hi:[1,0]
	v_exp_f32_e32 v6, v6
	v_exp_f32_e32 v0, v0
	v_exp_f32_e32 v1, v1
	v_exp_f32_e32 v7, v7
	v_add_co_u32_e32 v2, vcc, s21, v96
	v_pk_fma_f32 v[0:1], v[0:1], s[22:23], s[22:23] op_sel_hi:[1,0,0]
	s_nop 0
	v_addc_co_u32_e32 v3, vcc, 0, v97, vcc
	v_rcp_f32_e32 v0, v0
	v_rcp_f32_e32 v1, v1
	global_store_dwordx2 v[2:3], v[4:5], off
	v_pk_mul_f32 v[4:5], v[88:89], v[92:93]
	v_pk_mul_f32 v[2:3], v[90:91], v[94:95]
	v_pk_mul_f32 v[0:1], v[0:1], v[4:5]
	v_pk_fma_f32 v[4:5], v[6:7], s[22:23], s[22:23] op_sel_hi:[1,0,0]
	v_pk_mul_f32 v[6:7], v[80:81], s[20:21] op_sel_hi:[1,0]
	v_rcp_f32_e32 v4, v4
	v_rcp_f32_e32 v5, v5
	v_exp_f32_e32 v6, v6
	v_exp_f32_e32 v7, v7
	v_pk_mul_f32 v[10:11], v[82:83], s[20:21] op_sel_hi:[1,0]
	v_pk_mul_f32 v[2:3], v[4:5], v[2:3]
	v_exp_f32_e32 v10, v10
	v_pk_fma_f32 v[4:5], v[6:7], s[22:23], s[22:23] op_sel_hi:[1,0,0]
	v_exp_f32_e32 v11, v11
	v_rcp_f32_e32 v4, v4
	v_rcp_f32_e32 v5, v5
	v_pk_mul_f32 v[8:9], v[80:81], v[84:85]
	v_pk_mul_f32 v[6:7], v[82:83], v[86:87]
	v_pk_mul_f32 v[14:15], v[74:75], s[20:21] op_sel_hi:[1,0]
	v_pk_mul_f32 v[4:5], v[4:5], v[8:9]
	v_pk_fma_f32 v[8:9], v[10:11], s[22:23], s[22:23] op_sel_hi:[1,0,0]
	v_pk_mul_f32 v[10:11], v[72:73], s[20:21] op_sel_hi:[1,0]
	v_rcp_f32_e32 v8, v8
	v_rcp_f32_e32 v9, v9
	v_exp_f32_e32 v10, v10
	v_exp_f32_e32 v11, v11
	v_exp_f32_e32 v14, v14
	v_pk_mul_f32 v[6:7], v[8:9], v[6:7]
	v_exp_f32_e32 v15, v15
	v_pk_fma_f32 v[8:9], v[10:11], s[22:23], s[22:23] op_sel_hi:[1,0,0]
	v_pk_mul_f32 v[12:13], v[72:73], v[76:77]
	v_rcp_f32_e32 v8, v8
	v_rcp_f32_e32 v9, v9
	v_pk_mul_f32 v[10:11], v[74:75], v[78:79]
	v_pk_mul_f32 v[18:19], v[66:67], s[20:21] op_sel_hi:[1,0]
	v_pk_mul_f32 v[16:17], v[64:65], v[68:69]
	v_pk_mul_f32 v[8:9], v[8:9], v[12:13]
	v_pk_fma_f32 v[12:13], v[14:15], s[22:23], s[22:23] op_sel_hi:[1,0,0]
	v_pk_mul_f32 v[14:15], v[64:65], s[20:21] op_sel_hi:[1,0]
	v_rcp_f32_e32 v12, v12
	v_rcp_f32_e32 v13, v13
	v_exp_f32_e32 v14, v14
	v_exp_f32_e32 v15, v15
	v_exp_f32_e32 v18, v18
	v_pk_mul_f32 v[10:11], v[12:13], v[10:11]
	v_exp_f32_e32 v19, v19
	v_pk_fma_f32 v[12:13], v[14:15], s[22:23], s[22:23] op_sel_hi:[1,0,0]
	v_pk_mul_f32 v[14:15], v[66:67], v[70:71]
	v_rcp_f32_e32 v12, v12
	v_rcp_f32_e32 v13, v13
	v_pk_mul_f32 v[22:23], v[58:59], s[20:21] op_sel_hi:[1,0]
	v_pk_mul_f32 v[20:21], v[56:57], v[60:61]
	v_exp_f32_e32 v22, v22
	v_pk_mul_f32 v[12:13], v[12:13], v[16:17]
	v_pk_fma_f32 v[16:17], v[18:19], s[22:23], s[22:23] op_sel_hi:[1,0,0]
	v_pk_mul_f32 v[18:19], v[56:57], s[20:21] op_sel_hi:[1,0]
	v_rcp_f32_e32 v16, v16
	v_rcp_f32_e32 v17, v17
	v_exp_f32_e32 v18, v18
	v_exp_f32_e32 v19, v19
	v_exp_f32_e32 v23, v23
	v_pk_mul_f32 v[14:15], v[16:17], v[14:15]
	v_pk_mul_f32 v[26:27], v[50:51], s[20:21] op_sel_hi:[1,0]
	v_pk_fma_f32 v[16:17], v[18:19], s[22:23], s[22:23] op_sel_hi:[1,0,0]
	v_pk_mul_f32 v[18:19], v[58:59], v[62:63]
	v_rcp_f32_e32 v16, v16
	v_rcp_f32_e32 v17, v17
	v_exp_f32_e32 v26, v26
	v_exp_f32_e32 v27, v27
	v_pk_mul_f32 v[24:25], v[48:49], v[52:53]
	v_pk_mul_f32 v[16:17], v[16:17], v[20:21]
	v_pk_fma_f32 v[20:21], v[22:23], s[22:23], s[22:23] op_sel_hi:[1,0,0]
	v_pk_mul_f32 v[22:23], v[48:49], s[20:21] op_sel_hi:[1,0]
	v_rcp_f32_e32 v20, v20
	v_rcp_f32_e32 v21, v21
	v_exp_f32_e32 v22, v22
	v_exp_f32_e32 v23, v23
	v_pk_mul_f32 v[30:31], v[42:43], s[20:21] op_sel_hi:[1,0]
	v_pk_mul_f32 v[18:19], v[20:21], v[18:19]
	v_exp_f32_e32 v30, v30
	v_pk_fma_f32 v[20:21], v[22:23], s[22:23], s[22:23] op_sel_hi:[1,0,0]
	v_pk_mul_f32 v[22:23], v[50:51], v[54:55]
	v_rcp_f32_e32 v20, v20
	v_rcp_f32_e32 v21, v21
	v_exp_f32_e32 v31, v31
	v_pk_mul_f32 v[28:29], v[40:41], v[44:45]
	v_med3_f32 v0, v0, s40, v145
	v_pk_mul_f32 v[20:21], v[20:21], v[24:25]
	v_pk_fma_f32 v[24:25], v[26:27], s[22:23], s[22:23] op_sel_hi:[1,0,0]
	v_pk_mul_f32 v[26:27], v[40:41], s[20:21] op_sel_hi:[1,0]
	v_rcp_f32_e32 v24, v24
	v_rcp_f32_e32 v25, v25
	v_exp_f32_e32 v26, v26
	v_exp_f32_e32 v27, v27
	v_med3_f32 v1, v1, s40, v145
	v_pk_mul_f32 v[22:23], v[24:25], v[22:23]
	v_med3_f32 v2, v2, s40, v145
	v_pk_fma_f32 v[24:25], v[26:27], s[22:23], s[22:23] op_sel_hi:[1,0,0]
	v_pk_mul_f32 v[26:27], v[42:43], v[46:47]
	v_rcp_f32_e32 v24, v24
	v_rcp_f32_e32 v25, v25
	v_med3_f32 v3, v3, s40, v145
	v_med3_f32 v4, v4, s40, v145
	v_med3_f32 v5, v5, s40, v145
	v_pk_mul_f32 v[24:25], v[24:25], v[28:29]
	v_pk_fma_f32 v[28:29], v[30:31], s[22:23], s[22:23] op_sel_hi:[1,0,0]
	v_pk_mul_f32 v[30:31], v[32:33], s[20:21] op_sel_hi:[1,0]
	v_rcp_f32_e32 v28, v28
	v_rcp_f32_e32 v29, v29
	v_exp_f32_e32 v30, v30
	v_exp_f32_e32 v31, v31
	v_pk_mul_f32 v[32:33], v[32:33], v[36:37]
	v_pk_mul_f32 v[26:27], v[28:29], v[26:27]
	v_med3_f32 v6, v6, s40, v145
	v_pk_fma_f32 v[28:29], v[30:31], s[22:23], s[22:23] op_sel_hi:[1,0,0]
	v_pk_mul_f32 v[30:31], v[34:35], s[20:21] op_sel_hi:[1,0]
	v_rcp_f32_e32 v28, v28
	v_exp_f32_e32 v30, v30
	v_exp_f32_e32 v31, v31
	v_rcp_f32_e32 v29, v29
	v_pk_mul_f32 v[34:35], v[34:35], v[38:39]
	v_med3_f32 v7, v7, s40, v145
	v_pk_fma_f32 v[30:31], v[30:31], s[22:23], s[22:23] op_sel_hi:[1,0,0]
	v_pk_mul_f32 v[28:29], v[28:29], v[32:33]
	v_rcp_f32_e32 v30, v30
	v_rcp_f32_e32 v31, v31
	v_med3_f32 v8, v8, s40, v145
	v_med3_f32 v9, v9, s40, v145
	v_med3_f32 v10, v10, s40, v145
	v_pk_mul_f32 v[30:31], v[30:31], v[34:35]
	v_med3_f32 v11, v11, s40, v145
	v_med3_f32 v12, v12, s40, v145
	v_med3_f32 v13, v13, s40, v145
	v_med3_f32 v14, v14, s40, v145
	v_med3_f32 v15, v15, s40, v145
	v_med3_f32 v16, v16, s40, v145
	v_med3_f32 v17, v17, s40, v145
	v_med3_f32 v18, v18, s40, v145
	v_med3_f32 v19, v19, s40, v145
	v_med3_f32 v20, v20, s40, v145
	v_med3_f32 v21, v21, s40, v145
	v_med3_f32 v22, v22, s40, v145
	v_med3_f32 v23, v23, s40, v145
	v_med3_f32 v24, v24, s40, v145
	v_med3_f32 v25, v25, s40, v145
	v_med3_f32 v26, v26, s40, v145
	v_med3_f32 v27, v27, s40, v145
	v_med3_f32 v28, v28, s40, v145
	v_med3_f32 v29, v29, s40, v145
	v_med3_f32 v30, v30, s40, v145
	v_med3_f32 v31, v31, s40, v145
	v_permlane32_swap_b32_e32 v0, v16
	v_permlane32_swap_b32_e32 v8, v24
	v_permlane32_swap_b32_e32 v1, v17
	v_permlane32_swap_b32_e32 v9, v25
	v_permlane32_swap_b32_e32 v2, v18
	v_permlane32_swap_b32_e32 v10, v26
	v_permlane32_swap_b32_e32 v3, v19
	v_permlane32_swap_b32_e32 v11, v27
	v_permlane32_swap_b32_e32 v4, v20
	v_permlane32_swap_b32_e32 v12, v28
	v_permlane32_swap_b32_e32 v5, v21
	v_permlane32_swap_b32_e32 v13, v29
	v_permlane32_swap_b32_e32 v6, v22
	v_permlane32_swap_b32_e32 v14, v30
	v_permlane32_swap_b32_e32 v7, v23
	v_permlane32_swap_b32_e32 v15, v31
	v_permlane16_swap_b32_e32 v0, v8
	v_permlane16_swap_b32_e32 v16, v24
	v_permlane16_swap_b32_e32 v1, v9
	v_permlane16_swap_b32_e32 v17, v25
	v_permlane16_swap_b32_e32 v2, v10
	v_permlane16_swap_b32_e32 v18, v26
	v_permlane16_swap_b32_e32 v3, v11
	v_permlane16_swap_b32_e32 v19, v27
	v_permlane16_swap_b32_e32 v4, v12
	v_permlane16_swap_b32_e32 v20, v28
	v_permlane16_swap_b32_e32 v5, v13
	v_permlane16_swap_b32_e32 v21, v29
	v_permlane16_swap_b32_e32 v6, v14
	v_permlane16_swap_b32_e32 v22, v30
	v_permlane16_swap_b32_e32 v7, v15
	v_permlane16_swap_b32_e32 v23, v31
	v_cvt_scalef32_2xpk16_fp6_f32 v[0:5], v[0:15], v[16:31], 1.0
	v_add_co_u32_e32 v6, vcc, 0x2000, v98
	s_nop 1
	v_addc_co_u32_e32 v7, vcc, 0, v99, vcc
	global_store_dwordx4 v[6:7], v[0:3], off
	s_nop 1
	v_add_co_u32_e32 v0, vcc, 0x5000, v96
	s_nop 1
	v_addc_co_u32_e32 v1, vcc, 0, v97, vcc
	s_andn2_b64 vcc, exec, s[0:1]
	s_mov_b64 s[0:1], -1
	global_store_dwordx2 v[0:1], v[4:5], off
	s_cbranch_vccnz .LBB0_658
	s_andn2_b64 vcc, exec, s[14:15]
	s_cbranch_vccnz .LBB0_657
	s_branch .LBB0_657
.LBB0_666:
	s_andn2_b64 vcc, exec, s[16:17]
	s_cbranch_vccnz .Lp6_noext
	s_barrier
